# E2 epilogue: the 8 row-weight loads issued before the unit's K-loop (during accumulator zeroing) instead of at the epilogue top behind vmcnt(0); on top of spare-XCD conversion
# baseline (speedup 1.0000x reference)
; template <class Epi, class Sched, class AM, bool ALIGN_EPI = false, bool SP2 = false>
; __device__ __forceinline__ void gemm_phase(PG8_LAS unsigned char* lds, const Gemm g, const Sched& S, const Epi& E, const AM& am, const int wid_in) {
;     ...
; #pragma unroll
;         for (int a = 0; a < 2; ++a)
; #pragma unroll
;             for (int b = 0; b < 2; ++b)
; #pragma unroll
;                 for (int m = 0; m < 4; ++m)
; #pragma unroll
;                     for (int n = 0; n < 2; ++n) acc[a][b][m][n] = (f32x4){0.f, 0.f, 0.f, 0.f};
;         cur = nxt; cA = nA; cB = nB; ++ui;
;     __device__ __forceinline__ void operator()(const f32x4 (&acc)[2][2][4][2], const Unit& u, int wr, int wc, int fr, int fq) const {
;     ...
;         const int e = u.pb >> 2; const float* wrow = lw + (size_t)e * LISTCAP - rb[e];
;         float wv[2][4];
; #pragma unroll
;         for (int ai = 0; ai < 2; ++ai)
; #pragma unroll
;             for (int m = 0; m < 4; ++m) wv[ai][m] = wrow[row0 + ai * HALF + m * 16];
.LBB0_1649:
	s_ashr_i32 s13, s12, 31
	s_lshl_b64 s[16:17], s[12:13], 18
	s_add_u32 s16, s35, s16
	s_addc_u32 s17, s36, s17
	s_and_b64 s[20:21], s[18:19], exec
	s_cselect_b32 s13, s17, s27
	s_cselect_b32 s59, s16, s26
	s_ashr_i32 s15, s14, 31
	s_lshl_b64 s[20:21], s[14:15], 18
	s_add_u32 s20, s37, s20
	s_addc_u32 s21, s38, s21
	s_and_b64 s[30:31], s[18:19], exec
	s_cselect_b32 s15, s21, s29
	s_cselect_b32 s60, s20, s28
	s_add_u32 s26, s26, 0x20080
	s_addc_u32 s27, s27, 0
	s_add_u32 s61, s28, 0x100
	v_mov_b32_e32 v0, 0
	s_addc_u32 s62, s29, 0
	s_mov_b32 s63, -2
	v_mov_b32_e32 v1, v0
	v_mov_b32_e32 v2, v0
	v_mov_b32_e32 v3, v0
	v_mov_b32_e32 v4, v0
	v_mov_b32_e32 v5, v0
	v_mov_b32_e32 v6, v0
	v_mov_b32_e32 v7, v0
	v_mov_b32_e32 v16, v0
	v_mov_b32_e32 v17, v0
	v_mov_b32_e32 v18, v0
	v_mov_b32_e32 v19, v0
	v_mov_b32_e32 v20, v0
	v_mov_b32_e32 v21, v0
	v_mov_b32_e32 v22, v0
	v_mov_b32_e32 v23, v0
	v_mov_b32_e32 v32, v0
	v_mov_b32_e32 v33, v0
	v_mov_b32_e32 v34, v0
	v_mov_b32_e32 v35, v0
	v_mov_b32_e32 v36, v0
	v_mov_b32_e32 v37, v0
	v_mov_b32_e32 v38, v0
	v_mov_b32_e32 v39, v0
	v_mov_b32_e32 v48, v0
	v_mov_b32_e32 v49, v0
	v_mov_b32_e32 v50, v0
	v_mov_b32_e32 v51, v0
	v_mov_b32_e32 v52, v0
	v_mov_b32_e32 v53, v0
	v_mov_b32_e32 v54, v0
	v_mov_b32_e32 v55, v0
	v_mov_b32_e32 v8, v0
	v_mov_b32_e32 v9, v0
	v_mov_b32_e32 v10, v0
	v_mov_b32_e32 v11, v0
	v_mov_b32_e32 v12, v0
	v_mov_b32_e32 v13, v0
	v_mov_b32_e32 v14, v0
	v_mov_b32_e32 v15, v0
	v_mov_b32_e32 v24, v0
	v_mov_b32_e32 v25, v0
	v_mov_b32_e32 v26, v0
	v_mov_b32_e32 v27, v0
	v_mov_b32_e32 v28, v0
	v_mov_b32_e32 v29, v0
	v_mov_b32_e32 v30, v0
	v_mov_b32_e32 v31, v0
	v_mov_b32_e32 v40, v0
	v_mov_b32_e32 v41, v0
	v_mov_b32_e32 v42, v0
	v_mov_b32_e32 v43, v0
	v_mov_b32_e32 v44, v0
	v_mov_b32_e32 v45, v0
	v_mov_b32_e32 v46, v0
	v_mov_b32_e32 v47, v0
	v_mov_b32_e32 v56, v0
	v_mov_b32_e32 v57, v0
	v_mov_b32_e32 v58, v0
	v_mov_b32_e32 v59, v0
	v_mov_b32_e32 v60, v0
	v_mov_b32_e32 v61, v0
	v_mov_b32_e32 v62, v0
	v_mov_b32_e32 v63, v0
	v_mov_b32_e32 v64, v0
	v_mov_b32_e32 v65, v0
	v_mov_b32_e32 v66, v0
	v_mov_b32_e32 v67, v0
	v_mov_b32_e32 v68, v0
	v_mov_b32_e32 v69, v0
	v_mov_b32_e32 v70, v0
	v_mov_b32_e32 v71, v0
	v_mov_b32_e32 v72, v0
	v_mov_b32_e32 v73, v0
	v_mov_b32_e32 v74, v0
	v_mov_b32_e32 v75, v0
	v_mov_b32_e32 v80, v0
	v_mov_b32_e32 v81, v0
	v_mov_b32_e32 v82, v0
	v_mov_b32_e32 v83, v0
	v_mov_b32_e32 v88, v0
	v_mov_b32_e32 v89, v0
	v_mov_b32_e32 v90, v0
	v_mov_b32_e32 v91, v0
	v_mov_b32_e32 v92, v0
	v_mov_b32_e32 v93, v0
	v_mov_b32_e32 v94, v0
	v_mov_b32_e32 v95, v0
	v_mov_b32_e32 v104, v0
	v_mov_b32_e32 v105, v0
	v_mov_b32_e32 v106, v0
	v_mov_b32_e32 v107, v0
	v_mov_b32_e32 v108, v0
	v_mov_b32_e32 v109, v0
	v_mov_b32_e32 v110, v0
	v_mov_b32_e32 v111, v0
	v_mov_b32_e32 v76, v0
	v_mov_b32_e32 v77, v0
	v_mov_b32_e32 v78, v0
	v_mov_b32_e32 v79, v0
	v_mov_b32_e32 v84, v0
	v_mov_b32_e32 v85, v0
	v_mov_b32_e32 v86, v0
	v_mov_b32_e32 v87, v0
	v_mov_b32_e32 v96, v0
	v_mov_b32_e32 v97, v0
	v_mov_b32_e32 v98, v0
	v_mov_b32_e32 v99, v0
	v_mov_b32_e32 v100, v0
	v_mov_b32_e32 v101, v0
	v_mov_b32_e32 v102, v0
	v_mov_b32_e32 v103, v0
	v_mov_b32_e32 v112, v0
	v_mov_b32_e32 v113, v0
	v_mov_b32_e32 v114, v0
	v_mov_b32_e32 v115, v0
	v_mov_b32_e32 v116, v0
	v_mov_b32_e32 v117, v0
	v_mov_b32_e32 v118, v0
	v_mov_b32_e32 v119, v0
	v_mov_b32_e32 v120, v0
	v_mov_b32_e32 v121, v0
	v_mov_b32_e32 v122, v0
	v_mov_b32_e32 v123, v0
	v_mov_b32_e32 v124, v0
	v_mov_b32_e32 v125, v0
	v_mov_b32_e32 v126, v0
	v_mov_b32_e32 v127, v0
	s_ashr_i32 s98, s24, 2
	s_ashr_i32 s99, s98, 31
	s_lshl_b64 s[98:99], s[98:99], 18
	s_add_u32 s98, s45, s98
	s_addc_u32 s99, s46, s99
	s_and_b32 s100, s24, -4
	s_add_i32 s100, s100, 0x27c00
	v_mov_b32_e32 v252, s100
	ds_read_b32 v252, v252
	v_lshl_add_u32 v254, s22, 8, v149
	v_mov_b32_e32 v255, s99
	s_waitcnt lgkmcnt(0)
	v_ashrrev_i32_e32 v253, 31, v252
	v_lshlrev_b64 v[252:253], 2, v[252:253]
	v_sub_co_u32_e64 v252, s[100:101], s98, v252
	s_nop 1
	v_subb_co_u32_e64 v253, s[100:101], v255, v253, s[100:101]
	v_ashrrev_i32_e32 v255, 31, v254
	v_lshl_add_u64 v[252:253], v[254:255], 2, v[252:253]
	global_load_dword v232, v[252:253], off
	global_load_dword v234, v[252:253], off offset:64
	global_load_dword v236, v[252:253], off offset:128
	global_load_dword v238, v[252:253], off offset:192
	global_load_dword v240, v[252:253], off offset:512
	global_load_dword v242, v[252:253], off offset:576
	global_load_dword v244, v[252:253], off offset:640
	global_load_dword v246, v[252:253], off offset:704

; __device__ __forceinline__ u32x4 pack8(const f32x4 v0, const f32x4 v1) { u32x4 w; w.x = cvt_pk_bf16(v0[0], v0[1]); w.y = cvt_pk_bf16(v0[2], v0[3]); w.z = cvt_pk_bf16(v1[0], v1[1]); w.w = cvt_pk_bf16(v1[2], v1[3]); return w; }
;     __device__ __forceinline__ void operator()(const f32x4 (&acc)[2][2][4][2], const Unit& u, int wr, int wc, int fr, int fq) const {
;     ...
; #pragma unroll
;         for (int ai = 0; ai < 2; ++ai)
; #pragma unroll
;             for (int m = 0; m < 4; ++m) {
;                 const int row = row0 + ai * HALF + m * 16; const float w = wv[ai][m];
; #pragma unroll
;                 for (int bj = 0; bj < 2; ++bj) *(u32x4*)(O + (size_t)(row - fr + tr_) * D + col0 - 8 * fq + 8 * tq_ + bj * HALF) = xpose4x16(pack8(acc[ai][bj][m][0] * w, acc[ai][bj][m][1] * w), sa_);
;             }
.LBB0_1653:
	s_ashr_i32 s26, s24, 2
	s_ashr_i32 s27, s26, 31
	s_lshl_b64 s[26:27], s[26:27], 18
	s_add_u32 s13, s45, s26
	s_addc_u32 s15, s46, s27
	s_and_b32 s24, s24, -4
	s_add_i32 s24, s24, 0
	s_add_i32 s24, s24, 0x27c00
	v_mov_b32_e32 v144, s24
	ds_read_b32 v144, v144
	v_lshl_add_u32 v146, s22, 8, v149
	v_mov_b32_e32 v147, s15
	v_lshl_add_u32 v164, s58, 8, v153
	v_ashrrev_i32_e32 v165, 31, v164
	s_waitcnt lgkmcnt(0)
	v_ashrrev_i32_e32 v145, 31, v144
	v_lshlrev_b64 v[144:145], 2, v[144:145]
	v_sub_co_u32_e32 v144, vcc, s13, v144
	s_nop 1
	v_subb_co_u32_e32 v145, vcc, v147, v145, vcc
	v_ashrrev_i32_e32 v147, 31, v146
	v_lshl_add_u64 v[162:163], v[146:147], 2, v[144:145]
	v_add_u32_e32 v144, v146, v157
	v_ashrrev_i32_e32 v145, 31, v144
	v_lshlrev_b64 v[170:171], 11, v[144:145]
	v_lshlrev_b64 v[146:147], 1, v[164:165]
	v_lshl_add_u64 v[170:171], s[6:7], 0, v[170:171]
	v_lshl_add_u64 v[170:171], v[170:171], 0, v[146:147]
	v_lshl_add_u64 v[170:171], v[170:171], 0, v[142:143]
	v_lshl_add_u64 v[170:171], v[170:171], 0, v[136:137]
	v_add_u32_e32 v164, 16, v144
	v_ashrrev_i32_e32 v165, 31, v164
	v_lshlrev_b64 v[164:165], 11, v[164:165]
	v_lshl_add_u64 v[164:165], s[6:7], 0, v[164:165]
	v_lshl_add_u64 v[164:165], v[164:165], 0, v[146:147]
	v_lshl_add_u64 v[164:165], v[164:165], 0, v[142:143]
	v_lshl_add_u64 v[164:165], v[164:165], 0, v[136:137]
	v_add_u32_e32 v166, 32, v144
	v_ashrrev_i32_e32 v167, 31, v166
	v_lshlrev_b64 v[166:167], 11, v[166:167]
	v_lshl_add_u64 v[166:167], s[6:7], 0, v[166:167]
	v_lshl_add_u64 v[166:167], v[166:167], 0, v[146:147]
	v_lshl_add_u64 v[166:167], v[166:167], 0, v[142:143]
	v_lshl_add_u64 v[166:167], v[166:167], 0, v[136:137]
	v_add_u32_e32 v168, 48, v144
	v_ashrrev_i32_e32 v169, 31, v168
	s_andn2_b64 vcc, exec, s[18:19]
	s_mov_b64 s[18:19], -1
	s_waitcnt vmcnt(0)
	v_pk_mul_f32 v[84:85], v[84:85], v[238:239] op_sel_hi:[1,0]
	v_pk_mul_f32 v[126:127], v[126:127], v[232:233] op_sel_hi:[1,0]
	v_pk_mul_f32 v[124:125], v[124:125], v[232:233] op_sel_hi:[1,0]
	v_pk_mul_f32 v[122:123], v[122:123], v[232:233] op_sel_hi:[1,0]
	v_pk_mul_f32 v[120:121], v[120:121], v[232:233] op_sel_hi:[1,0]
	v_cvt_pk_bf16_f32 v124, v124, v125
	v_cvt_pk_bf16_f32 v125, v126, v127
	v_pk_mul_f32 v[110:111], v[110:111], v[232:233] op_sel_hi:[1,0]
	v_cvt_pk_bf16_f32 v126, v120, v121
	v_cvt_pk_bf16_f32 v123, v122, v123
	ds_bpermute_b32 v120, v155, v124
	ds_bpermute_b32 v121, v155, v125
	ds_bpermute_b32 v122, v155, v126
	ds_bpermute_b32 v123, v155, v123
	v_pk_mul_f32 v[108:109], v[108:109], v[232:233] op_sel_hi:[1,0]
	v_pk_mul_f32 v[106:107], v[106:107], v[232:233] op_sel_hi:[1,0]
	v_pk_mul_f32 v[104:105], v[104:105], v[232:233] op_sel_hi:[1,0]
	v_pk_mul_f32 v[114:115], v[114:115], v[234:235] op_sel_hi:[1,0]
	s_waitcnt lgkmcnt(0)
	global_store_dwordx4 v[170:171], v[120:123], off
	v_cvt_pk_bf16_f32 v108, v108, v109
	v_cvt_pk_bf16_f32 v109, v110, v111
	v_cvt_pk_bf16_f32 v110, v104, v105
	v_cvt_pk_bf16_f32 v107, v106, v107
	ds_bpermute_b32 v104, v155, v108
	ds_bpermute_b32 v105, v155, v109
	ds_bpermute_b32 v106, v155, v110
	ds_bpermute_b32 v107, v155, v107
	v_pk_mul_f32 v[108:109], v[118:119], v[234:235] op_sel_hi:[1,0]
	v_pk_mul_f32 v[110:111], v[116:117], v[234:235] op_sel_hi:[1,0]
	v_pk_mul_f32 v[112:113], v[112:113], v[234:235] op_sel_hi:[1,0]
	v_pk_mul_f32 v[94:95], v[94:95], v[234:235] op_sel_hi:[1,0]
	s_waitcnt lgkmcnt(0)
	global_store_dwordx4 v[170:171], v[104:107], off offset:256
	v_pk_mul_f32 v[92:93], v[92:93], v[234:235] op_sel_hi:[1,0]
	v_pk_mul_f32 v[90:91], v[90:91], v[234:235] op_sel_hi:[1,0]
	v_cvt_pk_bf16_f32 v104, v110, v111
	v_cvt_pk_bf16_f32 v105, v108, v109
	v_cvt_pk_bf16_f32 v106, v112, v113
	v_cvt_pk_bf16_f32 v107, v114, v115
	ds_bpermute_b32 v104, v155, v104
	ds_bpermute_b32 v105, v155, v105
	ds_bpermute_b32 v106, v155, v106
	ds_bpermute_b32 v107, v155, v107
	v_pk_mul_f32 v[88:89], v[88:89], v[234:235] op_sel_hi:[1,0]
	v_pk_mul_f32 v[98:99], v[98:99], v[236:237] op_sel_hi:[1,0]
	v_pk_mul_f32 v[96:97], v[96:97], v[236:237] op_sel_hi:[1,0]
	v_pk_mul_f32 v[82:83], v[82:83], v[236:237] op_sel_hi:[1,0]
	s_waitcnt lgkmcnt(0)
	global_store_dwordx4 v[164:165], v[104:107], off
	v_cvt_pk_bf16_f32 v92, v92, v93
	v_cvt_pk_bf16_f32 v93, v94, v95
	v_cvt_pk_bf16_f32 v94, v88, v89
	v_cvt_pk_bf16_f32 v91, v90, v91
	ds_bpermute_b32 v88, v155, v92
	ds_bpermute_b32 v89, v155, v93
	ds_bpermute_b32 v90, v155, v94
	ds_bpermute_b32 v91, v155, v91
	v_pk_mul_f32 v[92:93], v[102:103], v[236:237] op_sel_hi:[1,0]
	v_pk_mul_f32 v[94:95], v[100:101], v[236:237] op_sel_hi:[1,0]
	v_pk_mul_f32 v[80:81], v[80:81], v[236:237] op_sel_hi:[1,0]
	v_pk_mul_f32 v[74:75], v[74:75], v[236:237] op_sel_hi:[1,0]
	s_waitcnt lgkmcnt(0)
	global_store_dwordx4 v[164:165], v[88:91], off offset:256
	v_pk_mul_f32 v[72:73], v[72:73], v[236:237] op_sel_hi:[1,0]
	v_pk_mul_f32 v[70:71], v[70:71], v[238:239] op_sel_hi:[1,0]
	v_cvt_pk_bf16_f32 v88, v94, v95
	v_cvt_pk_bf16_f32 v89, v92, v93
	v_cvt_pk_bf16_f32 v90, v96, v97
	v_cvt_pk_bf16_f32 v91, v98, v99
	ds_bpermute_b32 v88, v155, v88
	ds_bpermute_b32 v89, v155, v89
	ds_bpermute_b32 v90, v155, v90
	ds_bpermute_b32 v91, v155, v91
	v_pk_mul_f32 v[68:69], v[68:69], v[238:239] op_sel_hi:[1,0]
	v_pk_mul_f32 v[66:67], v[66:67], v[238:239] op_sel_hi:[1,0]
	v_pk_mul_f32 v[64:65], v[64:65], v[238:239] op_sel_hi:[1,0]
	v_pk_mul_f32 v[62:63], v[62:63], v[240:241] op_sel_hi:[1,0]
	s_waitcnt lgkmcnt(0)
; __device__ __forceinline__ u32x4 pack8(const f32x4 v0, const f32x4 v1) { u32x4 w; w.x = cvt_pk_bf16(v0[0], v0[1]); w.y = cvt_pk_bf16(v0[2], v0[3]); w.z = cvt_pk_bf16(v1[0], v1[1]); w.w = cvt_pk_bf16(v1[2], v1[3]); return w; }
;     __device__ __forceinline__ void operator()(const f32x4 (&acc)[2][2][4][2], const Unit& u, int wr, int wc, int fr, int fq) const {
;     ...
; #pragma unroll
;         for (int ai = 0; ai < 2; ++ai)
; #pragma unroll
;             for (int m = 0; m < 4; ++m) {
;                 const int row = row0 + ai * HALF + m * 16; const float w = wv[ai][m];
; #pragma unroll
;                 for (int bj = 0; bj < 2; ++bj) *(u32x4*)(O + (size_t)(row - fr + tr_) * D + col0 - 8 * fq + 8 * tq_ + bj * HALF) = xpose4x16(pack8(acc[ai][bj][m][0] * w, acc[ai][bj][m][1] * w), sa_);
;             }
	global_store_dwordx4 v[166:167], v[88:91], off
	v_cvt_pk_bf16_f32 v80, v80, v81
	v_cvt_pk_bf16_f32 v81, v82, v83
	v_cvt_pk_bf16_f32 v82, v72, v73
	v_cvt_pk_bf16_f32 v75, v74, v75
	ds_bpermute_b32 v72, v155, v80
	ds_bpermute_b32 v73, v155, v81
	ds_bpermute_b32 v74, v155, v82
	ds_bpermute_b32 v75, v155, v75
	v_pk_mul_f32 v[82:83], v[86:87], v[238:239] op_sel_hi:[1,0]
	v_lshlrev_b64 v[80:81], 11, v[168:169]
	v_pk_mul_f32 v[60:61], v[60:61], v[240:241] op_sel_hi:[1,0]
	v_pk_mul_f32 v[58:59], v[58:59], v[240:241] op_sel_hi:[1,0]
	s_waitcnt lgkmcnt(0)
	global_store_dwordx4 v[166:167], v[72:75], off offset:256
	v_pk_mul_f32 v[56:57], v[56:57], v[240:241] op_sel_hi:[1,0]
	v_pk_mul_f32 v[54:55], v[54:55], v[240:241] op_sel_hi:[1,0]
	v_pk_mul_f32 v[74:75], v[76:77], v[238:239] op_sel_hi:[1,0]
	v_pk_mul_f32 v[72:73], v[78:79], v[238:239] op_sel_hi:[1,0]
	v_cvt_pk_bf16_f32 v76, v84, v85
	v_cvt_pk_bf16_f32 v77, v82, v83
	v_cvt_pk_bf16_f32 v74, v74, v75
	ds_bpermute_b32 v74, v155, v74
	v_cvt_pk_bf16_f32 v75, v72, v73
	ds_bpermute_b32 v72, v155, v76
	ds_bpermute_b32 v73, v155, v77
	ds_bpermute_b32 v75, v155, v75
	v_lshl_add_u64 v[76:77], s[6:7], 0, v[80:81]
	v_lshl_add_u64 v[76:77], v[76:77], 0, v[146:147]
	v_lshl_add_u64 v[76:77], v[76:77], 0, v[142:143]
	v_lshl_add_u64 v[76:77], v[76:77], 0, v[136:137]
	s_waitcnt lgkmcnt(0)
	global_store_dwordx4 v[76:77], v[72:75], off
	v_cvt_pk_bf16_f32 v68, v68, v69
	v_cvt_pk_bf16_f32 v69, v70, v71
	v_cvt_pk_bf16_f32 v70, v64, v65
	v_cvt_pk_bf16_f32 v67, v66, v67
	ds_bpermute_b32 v64, v155, v68
	ds_bpermute_b32 v65, v155, v69
	ds_bpermute_b32 v66, v155, v70
	ds_bpermute_b32 v67, v155, v67
	v_pk_mul_f32 v[52:53], v[52:53], v[240:241] op_sel_hi:[1,0]
	v_pk_mul_f32 v[50:51], v[50:51], v[240:241] op_sel_hi:[1,0]
	v_pk_mul_f32 v[48:49], v[48:49], v[240:241] op_sel_hi:[1,0]
	v_pk_mul_f32 v[46:47], v[46:47], v[242:243] op_sel_hi:[1,0]
	s_waitcnt lgkmcnt(0)
	global_store_dwordx4 v[76:77], v[64:67], off offset:256
	v_cvt_pk_bf16_f32 v60, v60, v61
	v_cvt_pk_bf16_f32 v61, v62, v63
	v_cvt_pk_bf16_f32 v62, v56, v57
	v_cvt_pk_bf16_f32 v59, v58, v59
	ds_bpermute_b32 v56, v155, v60
	s_nop 0
	v_add_u32_e32 v64, 0x80, v144
	v_ashrrev_i32_e32 v65, 31, v64
	v_lshlrev_b64 v[64:65], 11, v[64:65]
	ds_bpermute_b32 v57, v155, v61
	ds_bpermute_b32 v58, v155, v62
	ds_bpermute_b32 v59, v155, v59
	v_lshl_add_u64 v[60:61], s[6:7], 0, v[64:65]
	v_lshl_add_u64 v[60:61], v[60:61], 0, v[146:147]
	v_lshl_add_u64 v[60:61], v[60:61], 0, v[142:143]
	v_lshl_add_u64 v[60:61], v[60:61], 0, v[136:137]
	s_waitcnt lgkmcnt(0)
	global_store_dwordx4 v[60:61], v[56:59], off
	v_cvt_pk_bf16_f32 v52, v52, v53
	v_cvt_pk_bf16_f32 v53, v54, v55
	v_cvt_pk_bf16_f32 v54, v48, v49
	v_cvt_pk_bf16_f32 v51, v50, v51
	ds_bpermute_b32 v48, v155, v52
	ds_bpermute_b32 v49, v155, v53
	ds_bpermute_b32 v50, v155, v54
	ds_bpermute_b32 v51, v155, v51
	v_pk_mul_f32 v[44:45], v[44:45], v[242:243] op_sel_hi:[1,0]
	v_pk_mul_f32 v[42:43], v[42:43], v[242:243] op_sel_hi:[1,0]
	v_pk_mul_f32 v[40:41], v[40:41], v[242:243] op_sel_hi:[1,0]
	v_pk_mul_f32 v[38:39], v[38:39], v[242:243] op_sel_hi:[1,0]
	s_waitcnt lgkmcnt(0)
	global_store_dwordx4 v[60:61], v[48:51], off offset:256
	v_cvt_pk_bf16_f32 v44, v44, v45
	v_cvt_pk_bf16_f32 v45, v46, v47
	v_cvt_pk_bf16_f32 v46, v40, v41
	v_cvt_pk_bf16_f32 v43, v42, v43
	ds_bpermute_b32 v40, v155, v44
	s_nop 0
	v_add_u32_e32 v48, 0x90, v144
	v_ashrrev_i32_e32 v49, 31, v48
	v_lshlrev_b64 v[48:49], 11, v[48:49]
	ds_bpermute_b32 v41, v155, v45
	ds_bpermute_b32 v42, v155, v46
	ds_bpermute_b32 v43, v155, v43
	v_lshl_add_u64 v[44:45], s[6:7], 0, v[48:49]
	v_lshl_add_u64 v[44:45], v[44:45], 0, v[146:147]
	v_lshl_add_u64 v[44:45], v[44:45], 0, v[142:143]
	v_lshl_add_u64 v[44:45], v[44:45], 0, v[136:137]
	v_pk_mul_f32 v[36:37], v[36:37], v[242:243] op_sel_hi:[1,0]
	v_pk_mul_f32 v[34:35], v[34:35], v[242:243] op_sel_hi:[1,0]
	s_waitcnt lgkmcnt(0)
; #define PG8_BAR __builtin_amdgcn_s_barrier()
; __device__ __forceinline__ u32x4 pack8(const f32x4 v0, const f32x4 v1) { u32x4 w; w.x = cvt_pk_bf16(v0[0], v0[1]); w.y = cvt_pk_bf16(v0[2], v0[3]); w.z = cvt_pk_bf16(v1[0], v1[1]); w.w = cvt_pk_bf16(v1[2], v1[3]); return w; }
; template <class Epi, class Sched, class AM, bool ALIGN_EPI = false, bool SP2 = false>
; __device__ __forceinline__ void gemm_phase(PG8_LAS unsigned char* lds, const Gemm g, const Sched& S, const Epi& E, const AM& am, const int wid_in) {
;     ...
;         if (!has_next) break;
; #pragma unroll
;         for (int a = 0; a < 2; ++a)
; #pragma unroll
;             for (int b = 0; b < 2; ++b)
; #pragma unroll
;                 for (int m = 0; m < 4; ++m)
; #pragma unroll
;                     for (int n = 0; n < 2; ++n) acc[a][b][m][n] = (f32x4){0.f, 0.f, 0.f, 0.f};
;         cur = nxt; cA = nA; cB = nB; ++ui;
;         if constexpr (AM::GATHER) { _Pragma("unroll") for (int h = 0; h < 2; ++h) _Pragma("unroll") for (int i = 0; i < 2; ++i) gao[h][i] = gno[h][i]; }
;         if constexpr (ALIGN_EPI) { if (wr == 1) PG8_BAR; }
;     __device__ __forceinline__ void operator()(const f32x4 (&acc)[2][2][4][2], const Unit& u, int wr, int wc, int fr, int fq) const {
;     ...
; #pragma unroll
;         for (int ai = 0; ai < 2; ++ai)
; #pragma unroll
;             for (int m = 0; m < 4; ++m) {
;                 const int row = row0 + ai * HALF + m * 16; const float w = wv[ai][m];
; #pragma unroll
;                 for (int bj = 0; bj < 2; ++bj) *(u32x4*)(O + (size_t)(row - fr + tr_) * D + col0 - 8 * fq + 8 * tq_ + bj * HALF) = xpose4x16(pack8(acc[ai][bj][m][0] * w, acc[ai][bj][m][1] * w), sa_);
;             }
	global_store_dwordx4 v[44:45], v[40:43], off
	v_pk_mul_f32 v[32:33], v[32:33], v[242:243] op_sel_hi:[1,0]
	v_cvt_pk_bf16_f32 v36, v36, v37
	v_cvt_pk_bf16_f32 v37, v38, v39
	v_pk_mul_f32 v[30:31], v[30:31], v[244:245] op_sel_hi:[1,0]
	v_cvt_pk_bf16_f32 v38, v32, v33
	v_cvt_pk_bf16_f32 v35, v34, v35
	ds_bpermute_b32 v32, v155, v36
	ds_bpermute_b32 v33, v155, v37
	ds_bpermute_b32 v34, v155, v38
	ds_bpermute_b32 v35, v155, v35
	v_pk_mul_f32 v[28:29], v[28:29], v[244:245] op_sel_hi:[1,0]
	v_pk_mul_f32 v[26:27], v[26:27], v[244:245] op_sel_hi:[1,0]
	v_pk_mul_f32 v[24:25], v[24:25], v[244:245] op_sel_hi:[1,0]
	v_pk_mul_f32 v[22:23], v[22:23], v[244:245] op_sel_hi:[1,0]
	s_waitcnt lgkmcnt(0)
	global_store_dwordx4 v[44:45], v[32:35], off offset:256
	v_cvt_pk_bf16_f32 v28, v28, v29
	v_cvt_pk_bf16_f32 v29, v30, v31
	v_cvt_pk_bf16_f32 v30, v24, v25
	v_cvt_pk_bf16_f32 v27, v26, v27
	ds_bpermute_b32 v24, v155, v28
	s_nop 0
	v_add_u32_e32 v32, 0xa0, v144
	v_ashrrev_i32_e32 v33, 31, v32
	v_lshlrev_b64 v[32:33], 11, v[32:33]
	ds_bpermute_b32 v25, v155, v29
	ds_bpermute_b32 v26, v155, v30
	ds_bpermute_b32 v27, v155, v27
	v_lshl_add_u64 v[28:29], s[6:7], 0, v[32:33]
	v_lshl_add_u64 v[28:29], v[28:29], 0, v[146:147]
	v_lshl_add_u64 v[28:29], v[28:29], 0, v[142:143]
	v_lshl_add_u64 v[28:29], v[28:29], 0, v[136:137]
	v_pk_mul_f32 v[20:21], v[20:21], v[244:245] op_sel_hi:[1,0]
	v_pk_mul_f32 v[18:19], v[18:19], v[244:245] op_sel_hi:[1,0]
	s_waitcnt lgkmcnt(0)
	global_store_dwordx4 v[28:29], v[24:27], off
	v_pk_mul_f32 v[16:17], v[16:17], v[244:245] op_sel_hi:[1,0]
	v_cvt_pk_bf16_f32 v20, v20, v21
	v_cvt_pk_bf16_f32 v21, v22, v23
	v_pk_mul_f32 v[14:15], v[14:15], v[246:247] op_sel_hi:[1,0]
	v_cvt_pk_bf16_f32 v22, v16, v17
	v_cvt_pk_bf16_f32 v19, v18, v19
	ds_bpermute_b32 v16, v155, v20
	ds_bpermute_b32 v17, v155, v21
	ds_bpermute_b32 v18, v155, v22
	ds_bpermute_b32 v19, v155, v19
	v_pk_mul_f32 v[12:13], v[12:13], v[246:247] op_sel_hi:[1,0]
	v_pk_mul_f32 v[10:11], v[10:11], v[246:247] op_sel_hi:[1,0]
	v_pk_mul_f32 v[8:9], v[8:9], v[246:247] op_sel_hi:[1,0]
	v_pk_mul_f32 v[6:7], v[6:7], v[246:247] op_sel_hi:[1,0]
	s_waitcnt lgkmcnt(0)
	global_store_dwordx4 v[28:29], v[16:19], off offset:256
	v_cvt_pk_bf16_f32 v12, v12, v13
	v_cvt_pk_bf16_f32 v13, v14, v15
	v_cvt_pk_bf16_f32 v14, v8, v9
	v_cvt_pk_bf16_f32 v11, v10, v11
	ds_bpermute_b32 v8, v155, v12
	s_nop 0
	v_add_u32_e32 v16, 0xb0, v144
	v_ashrrev_i32_e32 v17, 31, v16
	v_lshlrev_b64 v[16:17], 11, v[16:17]
	ds_bpermute_b32 v9, v155, v13
	ds_bpermute_b32 v10, v155, v14
	ds_bpermute_b32 v11, v155, v11
	v_lshl_add_u64 v[12:13], s[6:7], 0, v[16:17]
	v_lshl_add_u64 v[12:13], v[12:13], 0, v[146:147]
	v_lshl_add_u64 v[12:13], v[12:13], 0, v[142:143]
	v_lshl_add_u64 v[12:13], v[12:13], 0, v[136:137]
	v_pk_mul_f32 v[4:5], v[4:5], v[246:247] op_sel_hi:[1,0]
	v_pk_mul_f32 v[2:3], v[2:3], v[246:247] op_sel_hi:[1,0]
	s_waitcnt lgkmcnt(0)
	global_store_dwordx4 v[12:13], v[8:11], off
	v_pk_mul_f32 v[0:1], v[0:1], v[246:247] op_sel_hi:[1,0]
	v_cvt_pk_bf16_f32 v4, v4, v5
	v_cvt_pk_bf16_f32 v5, v6, v7
	s_nop 0
	v_cvt_pk_bf16_f32 v6, v0, v1
	v_cvt_pk_bf16_f32 v3, v2, v3
	ds_bpermute_b32 v0, v155, v4
	ds_bpermute_b32 v1, v155, v5
	ds_bpermute_b32 v2, v155, v6
	ds_bpermute_b32 v3, v155, v3
	s_waitcnt lgkmcnt(0)
	global_store_dwordx4 v[12:13], v[0:3], off offset:256
	s_cbranch_vccnz .LBB0_1636
	s_andn2_b64 vcc, exec, s[2:3]
	s_cbranch_vccnz .LBB0_1635
	s_barrier
	s_branch .LBB0_1635

; template <class Epi, class Sched, class AM, bool ALIGN_EPI = false, bool SP2 = false>
; __device__ __forceinline__ void gemm_phase(PG8_LAS unsigned char* lds, const Gemm g, const Sched& S, const Epi& E, const AM& am, const int wid_in) {
;     ...
; #pragma unroll
;         for (int a = 0; a < 2; ++a)
; #pragma unroll
;             for (int b = 0; b < 2; ++b)
; #pragma unroll
;                 for (int m = 0; m < 4; ++m)
; #pragma unroll
;                     for (int n = 0; n < 2; ++n) acc[a][b][m][n] = (f32x4){0.f, 0.f, 0.f, 0.f};
;         cur = nxt; cA = nA; cB = nB; ++ui;
;     __device__ __forceinline__ void operator()(const f32x4 (&acc)[2][2][4][2], const Unit& u, int wr, int wc, int fr, int fq) const {
;     ...
;         const int e = u.pb >> 2; const float* wrow = lw + (size_t)e * LISTCAP - rb[e];
;         float wv[2][4];
; #pragma unroll
;         for (int ai = 0; ai < 2; ++ai)
; #pragma unroll
;             for (int m = 0; m < 4; ++m) wv[ai][m] = wrow[row0 + ai * HALF + m * 16];
.LBB0_2723:
	s_ashr_i32 s11, s10, 31
	s_lshl_b64 s[14:15], s[10:11], 18
	s_add_u32 s14, s31, s14
	s_addc_u32 s15, s34, s15
	s_and_b64 s[18:19], s[16:17], exec
	s_cselect_b32 s11, s15, s25
	s_cselect_b32 s57, s14, s24
	s_ashr_i32 s13, s12, 31
	s_lshl_b64 s[18:19], s[12:13], 18
	s_add_u32 s18, s35, s18
	s_addc_u32 s19, s36, s19
	s_and_b64 s[28:29], s[16:17], exec
	s_cselect_b32 s13, s19, s27
	s_cselect_b32 s58, s18, s26
	s_add_u32 s24, s24, 0x20080
	s_addc_u32 s25, s25, 0
	s_add_u32 s59, s26, 0x100
	v_mov_b32_e32 v0, 0
	s_addc_u32 s60, s27, 0
	s_mov_b32 s61, -2
	v_mov_b32_e32 v1, v0
	v_mov_b32_e32 v2, v0
	v_mov_b32_e32 v3, v0
	v_mov_b32_e32 v4, v0
	v_mov_b32_e32 v5, v0
	v_mov_b32_e32 v6, v0
	v_mov_b32_e32 v7, v0
	v_mov_b32_e32 v16, v0
	v_mov_b32_e32 v17, v0
	v_mov_b32_e32 v18, v0
	v_mov_b32_e32 v19, v0
	v_mov_b32_e32 v20, v0
	v_mov_b32_e32 v21, v0
	v_mov_b32_e32 v22, v0
	v_mov_b32_e32 v23, v0
	v_mov_b32_e32 v32, v0
	v_mov_b32_e32 v33, v0
	v_mov_b32_e32 v34, v0
	v_mov_b32_e32 v35, v0
	v_mov_b32_e32 v36, v0
	v_mov_b32_e32 v37, v0
	v_mov_b32_e32 v38, v0
	v_mov_b32_e32 v39, v0
	v_mov_b32_e32 v48, v0
	v_mov_b32_e32 v49, v0
	v_mov_b32_e32 v50, v0
	v_mov_b32_e32 v51, v0
	v_mov_b32_e32 v52, v0
	v_mov_b32_e32 v53, v0
	v_mov_b32_e32 v54, v0
	v_mov_b32_e32 v55, v0
	v_mov_b32_e32 v8, v0
	v_mov_b32_e32 v9, v0
	v_mov_b32_e32 v10, v0
	v_mov_b32_e32 v11, v0
	v_mov_b32_e32 v12, v0
	v_mov_b32_e32 v13, v0
	v_mov_b32_e32 v14, v0
	v_mov_b32_e32 v15, v0
	v_mov_b32_e32 v24, v0
	v_mov_b32_e32 v25, v0
	v_mov_b32_e32 v26, v0
	v_mov_b32_e32 v27, v0
	v_mov_b32_e32 v28, v0
	v_mov_b32_e32 v29, v0
	v_mov_b32_e32 v30, v0
	v_mov_b32_e32 v31, v0
	v_mov_b32_e32 v40, v0
	v_mov_b32_e32 v41, v0
	v_mov_b32_e32 v42, v0
	v_mov_b32_e32 v43, v0
	v_mov_b32_e32 v44, v0
	v_mov_b32_e32 v45, v0
	v_mov_b32_e32 v46, v0
	v_mov_b32_e32 v47, v0
	v_mov_b32_e32 v56, v0
	v_mov_b32_e32 v57, v0
	v_mov_b32_e32 v58, v0
	v_mov_b32_e32 v59, v0
	v_mov_b32_e32 v60, v0
	v_mov_b32_e32 v61, v0
	v_mov_b32_e32 v62, v0
	v_mov_b32_e32 v63, v0
	v_mov_b32_e32 v64, v0
	v_mov_b32_e32 v65, v0
	v_mov_b32_e32 v66, v0
	v_mov_b32_e32 v67, v0
	v_mov_b32_e32 v68, v0
	v_mov_b32_e32 v69, v0
	v_mov_b32_e32 v70, v0
	v_mov_b32_e32 v71, v0
	v_mov_b32_e32 v72, v0
	v_mov_b32_e32 v73, v0
	v_mov_b32_e32 v74, v0
	v_mov_b32_e32 v75, v0
	v_mov_b32_e32 v80, v0
	v_mov_b32_e32 v81, v0
	v_mov_b32_e32 v82, v0
	v_mov_b32_e32 v83, v0
	v_mov_b32_e32 v88, v0
	v_mov_b32_e32 v89, v0
	v_mov_b32_e32 v90, v0
	v_mov_b32_e32 v91, v0
	v_mov_b32_e32 v92, v0
	v_mov_b32_e32 v93, v0
	v_mov_b32_e32 v94, v0
	v_mov_b32_e32 v95, v0
	v_mov_b32_e32 v104, v0
	v_mov_b32_e32 v105, v0
	v_mov_b32_e32 v106, v0
	v_mov_b32_e32 v107, v0
	v_mov_b32_e32 v108, v0
	v_mov_b32_e32 v109, v0
	v_mov_b32_e32 v110, v0
	v_mov_b32_e32 v111, v0
	v_mov_b32_e32 v76, v0
	v_mov_b32_e32 v77, v0
	v_mov_b32_e32 v78, v0
	v_mov_b32_e32 v79, v0
	v_mov_b32_e32 v84, v0
	v_mov_b32_e32 v85, v0
	v_mov_b32_e32 v86, v0
	v_mov_b32_e32 v87, v0
	v_mov_b32_e32 v96, v0
	v_mov_b32_e32 v97, v0
	v_mov_b32_e32 v98, v0
	v_mov_b32_e32 v99, v0
	v_mov_b32_e32 v100, v0
	v_mov_b32_e32 v101, v0
	v_mov_b32_e32 v102, v0
	v_mov_b32_e32 v103, v0
	v_mov_b32_e32 v112, v0
	v_mov_b32_e32 v113, v0
	v_mov_b32_e32 v114, v0
	v_mov_b32_e32 v115, v0
	v_mov_b32_e32 v116, v0
	v_mov_b32_e32 v117, v0
	v_mov_b32_e32 v118, v0
	v_mov_b32_e32 v119, v0
	v_mov_b32_e32 v120, v0
	v_mov_b32_e32 v121, v0
	v_mov_b32_e32 v122, v0
	v_mov_b32_e32 v123, v0
	v_mov_b32_e32 v124, v0
	v_mov_b32_e32 v125, v0
	v_mov_b32_e32 v126, v0
	v_mov_b32_e32 v127, v0
	s_ashr_i32 s98, s22, 2
	s_ashr_i32 s99, s98, 31
	s_lshl_b64 s[98:99], s[98:99], 18
	s_add_u32 s98, s43, s98
	s_addc_u32 s99, s44, s99
	s_and_b32 s100, s22, -4
	s_add_i32 s100, s100, 0x27c00
	v_mov_b32_e32 v252, s100
	ds_read_b32 v252, v252
	v_lshl_add_u32 v254, s20, 8, v149
	v_mov_b32_e32 v255, s99
	s_waitcnt lgkmcnt(0)
	v_ashrrev_i32_e32 v253, 31, v252
	v_lshlrev_b64 v[252:253], 2, v[252:253]
	v_sub_co_u32_e64 v252, s[100:101], s98, v252
	s_nop 1
	v_subb_co_u32_e64 v253, s[100:101], v255, v253, s[100:101]
	v_ashrrev_i32_e32 v255, 31, v254
	v_lshl_add_u64 v[252:253], v[254:255], 2, v[252:253]
	global_load_dword v232, v[252:253], off
	global_load_dword v234, v[252:253], off offset:64
	global_load_dword v236, v[252:253], off offset:128
	global_load_dword v238, v[252:253], off offset:192
	global_load_dword v240, v[252:253], off offset:512
	global_load_dword v242, v[252:253], off offset:576
	global_load_dword v244, v[252:253], off offset:640
	global_load_dword v246, v[252:253], off offset:704

; __device__ __forceinline__ u32x4 pack8(const f32x4 v0, const f32x4 v1) { u32x4 w; w.x = cvt_pk_bf16(v0[0], v0[1]); w.y = cvt_pk_bf16(v0[2], v0[3]); w.z = cvt_pk_bf16(v1[0], v1[1]); w.w = cvt_pk_bf16(v1[2], v1[3]); return w; }
;     __device__ __forceinline__ void operator()(const f32x4 (&acc)[2][2][4][2], const Unit& u, int wr, int wc, int fr, int fq) const {
;         XPOSE_IDS();
;         const int row0 = u.pm * BM + wr * 64 + fr, col0 = u.pn * BM + wc * 32 + 8 * fq;
;         const int e = u.pb >> 2; const float* wrow = lw + (size_t)e * LISTCAP - rb[e];
;         float wv[2][4];
; #pragma unroll
;         for (int ai = 0; ai < 2; ++ai)
; #pragma unroll
;             for (int m = 0; m < 4; ++m) wv[ai][m] = wrow[row0 + ai * HALF + m * 16];
; #pragma unroll
;         for (int ai = 0; ai < 2; ++ai)
; #pragma unroll
;             for (int m = 0; m < 4; ++m) {
;                 const int row = row0 + ai * HALF + m * 16; const float w = wv[ai][m];
; #pragma unroll
;                 for (int bj = 0; bj < 2; ++bj) *(u32x4*)(O + (size_t)(row - fr + tr_) * D + col0 - 8 * fq + 8 * tq_ + bj * HALF) = xpose4x16(pack8(acc[ai][bj][m][0] * w, acc[ai][bj][m][1] * w), sa_);
.LBB0_2727:
	s_ashr_i32 s24, s22, 2
	s_ashr_i32 s25, s24, 31
	s_lshl_b64 s[24:25], s[24:25], 18
	s_add_u32 s11, s43, s24
	s_addc_u32 s13, s44, s25
	s_and_b32 s22, s22, -4
	s_add_i32 s22, s22, 0
	s_add_i32 s22, s22, 0x27c00
	v_mov_b32_e32 v144, s22
	ds_read_b32 v144, v144
	v_lshl_add_u32 v146, s20, 8, v149
	v_mov_b32_e32 v147, s13
	v_lshl_add_u32 v164, s56, 8, v153
	v_ashrrev_i32_e32 v165, 31, v164
	s_waitcnt lgkmcnt(0)
	v_ashrrev_i32_e32 v145, 31, v144
	v_lshlrev_b64 v[144:145], 2, v[144:145]
	v_sub_co_u32_e32 v144, vcc, s11, v144
	s_nop 1
	v_subb_co_u32_e32 v145, vcc, v147, v145, vcc
	v_ashrrev_i32_e32 v147, 31, v146
	v_lshl_add_u64 v[162:163], v[146:147], 2, v[144:145]
	v_add_u32_e32 v144, v146, v157
	v_ashrrev_i32_e32 v145, 31, v144
	v_lshlrev_b64 v[170:171], 11, v[144:145]
	v_lshlrev_b64 v[146:147], 1, v[164:165]
	v_lshl_add_u64 v[170:171], s[4:5], 0, v[170:171]
	v_lshl_add_u64 v[170:171], v[170:171], 0, v[146:147]
	v_lshl_add_u64 v[170:171], v[170:171], 0, v[142:143]
	v_lshl_add_u64 v[170:171], v[170:171], 0, v[136:137]
	v_add_u32_e32 v164, 16, v144
	v_ashrrev_i32_e32 v165, 31, v164
	v_lshlrev_b64 v[164:165], 11, v[164:165]
	v_lshl_add_u64 v[164:165], s[4:5], 0, v[164:165]
	v_lshl_add_u64 v[164:165], v[164:165], 0, v[146:147]
	v_lshl_add_u64 v[164:165], v[164:165], 0, v[142:143]
	v_lshl_add_u64 v[164:165], v[164:165], 0, v[136:137]
	v_add_u32_e32 v166, 32, v144
	v_ashrrev_i32_e32 v167, 31, v166
	v_lshlrev_b64 v[166:167], 11, v[166:167]
	v_lshl_add_u64 v[166:167], s[4:5], 0, v[166:167]
	v_lshl_add_u64 v[166:167], v[166:167], 0, v[146:147]
	v_lshl_add_u64 v[166:167], v[166:167], 0, v[142:143]
	v_lshl_add_u64 v[166:167], v[166:167], 0, v[136:137]
	v_add_u32_e32 v168, 48, v144
	v_ashrrev_i32_e32 v169, 31, v168
	s_andn2_b64 vcc, exec, s[16:17]
	s_mov_b64 s[16:17], -1
	s_waitcnt vmcnt(0)
	v_pk_mul_f32 v[84:85], v[84:85], v[238:239] op_sel_hi:[1,0]
	v_pk_mul_f32 v[126:127], v[126:127], v[232:233] op_sel_hi:[1,0]
	v_pk_mul_f32 v[124:125], v[124:125], v[232:233] op_sel_hi:[1,0]
	v_pk_mul_f32 v[122:123], v[122:123], v[232:233] op_sel_hi:[1,0]
	v_pk_mul_f32 v[120:121], v[120:121], v[232:233] op_sel_hi:[1,0]
	v_cvt_pk_bf16_f32 v124, v124, v125
	v_cvt_pk_bf16_f32 v125, v126, v127
	v_pk_mul_f32 v[110:111], v[110:111], v[232:233] op_sel_hi:[1,0]
	v_cvt_pk_bf16_f32 v126, v120, v121
	v_cvt_pk_bf16_f32 v123, v122, v123
	ds_bpermute_b32 v120, v155, v124
	ds_bpermute_b32 v121, v155, v125
	ds_bpermute_b32 v122, v155, v126
	ds_bpermute_b32 v123, v155, v123
	v_pk_mul_f32 v[108:109], v[108:109], v[232:233] op_sel_hi:[1,0]
	v_pk_mul_f32 v[106:107], v[106:107], v[232:233] op_sel_hi:[1,0]
	v_pk_mul_f32 v[104:105], v[104:105], v[232:233] op_sel_hi:[1,0]
	v_pk_mul_f32 v[114:115], v[114:115], v[234:235] op_sel_hi:[1,0]
	s_waitcnt lgkmcnt(0)
	global_store_dwordx4 v[170:171], v[120:123], off
	v_cvt_pk_bf16_f32 v108, v108, v109
	v_cvt_pk_bf16_f32 v109, v110, v111
	v_cvt_pk_bf16_f32 v110, v104, v105
	v_cvt_pk_bf16_f32 v107, v106, v107
	ds_bpermute_b32 v104, v155, v108
	ds_bpermute_b32 v105, v155, v109
	ds_bpermute_b32 v106, v155, v110
	ds_bpermute_b32 v107, v155, v107
	v_pk_mul_f32 v[108:109], v[118:119], v[234:235] op_sel_hi:[1,0]
	v_pk_mul_f32 v[110:111], v[116:117], v[234:235] op_sel_hi:[1,0]
	v_pk_mul_f32 v[112:113], v[112:113], v[234:235] op_sel_hi:[1,0]
	v_pk_mul_f32 v[94:95], v[94:95], v[234:235] op_sel_hi:[1,0]
	s_waitcnt lgkmcnt(0)
	global_store_dwordx4 v[170:171], v[104:107], off offset:256
	v_pk_mul_f32 v[92:93], v[92:93], v[234:235] op_sel_hi:[1,0]
	v_pk_mul_f32 v[90:91], v[90:91], v[234:235] op_sel_hi:[1,0]
	v_cvt_pk_bf16_f32 v104, v110, v111
	v_cvt_pk_bf16_f32 v105, v108, v109
	v_cvt_pk_bf16_f32 v106, v112, v113
	v_cvt_pk_bf16_f32 v107, v114, v115
	ds_bpermute_b32 v104, v155, v104
	ds_bpermute_b32 v105, v155, v105
	ds_bpermute_b32 v106, v155, v106
	ds_bpermute_b32 v107, v155, v107
	v_pk_mul_f32 v[88:89], v[88:89], v[234:235] op_sel_hi:[1,0]
	v_pk_mul_f32 v[98:99], v[98:99], v[236:237] op_sel_hi:[1,0]
	v_pk_mul_f32 v[96:97], v[96:97], v[236:237] op_sel_hi:[1,0]
	v_pk_mul_f32 v[82:83], v[82:83], v[236:237] op_sel_hi:[1,0]
	s_waitcnt lgkmcnt(0)
	global_store_dwordx4 v[164:165], v[104:107], off
	v_cvt_pk_bf16_f32 v92, v92, v93
	v_cvt_pk_bf16_f32 v93, v94, v95
	v_cvt_pk_bf16_f32 v94, v88, v89
	v_cvt_pk_bf16_f32 v91, v90, v91
	ds_bpermute_b32 v88, v155, v92
	ds_bpermute_b32 v89, v155, v93
	ds_bpermute_b32 v90, v155, v94
	ds_bpermute_b32 v91, v155, v91
	v_pk_mul_f32 v[92:93], v[102:103], v[236:237] op_sel_hi:[1,0]
	v_pk_mul_f32 v[94:95], v[100:101], v[236:237] op_sel_hi:[1,0]
	v_pk_mul_f32 v[80:81], v[80:81], v[236:237] op_sel_hi:[1,0]
	v_pk_mul_f32 v[74:75], v[74:75], v[236:237] op_sel_hi:[1,0]
	s_waitcnt lgkmcnt(0)
	global_store_dwordx4 v[164:165], v[88:91], off offset:256
	v_pk_mul_f32 v[72:73], v[72:73], v[236:237] op_sel_hi:[1,0]
	v_pk_mul_f32 v[70:71], v[70:71], v[238:239] op_sel_hi:[1,0]
	v_cvt_pk_bf16_f32 v88, v94, v95
	v_cvt_pk_bf16_f32 v89, v92, v93
	v_cvt_pk_bf16_f32 v90, v96, v97
	v_cvt_pk_bf16_f32 v91, v98, v99
	ds_bpermute_b32 v88, v155, v88
	ds_bpermute_b32 v89, v155, v89
	ds_bpermute_b32 v90, v155, v90
	ds_bpermute_b32 v91, v155, v91
	v_pk_mul_f32 v[68:69], v[68:69], v[238:239] op_sel_hi:[1,0]
	v_pk_mul_f32 v[66:67], v[66:67], v[238:239] op_sel_hi:[1,0]
	v_pk_mul_f32 v[64:65], v[64:65], v[238:239] op_sel_hi:[1,0]
	v_pk_mul_f32 v[62:63], v[62:63], v[240:241] op_sel_hi:[1,0]
	s_waitcnt lgkmcnt(0)
; __device__ __forceinline__ u32x4 pack8(const f32x4 v0, const f32x4 v1) { u32x4 w; w.x = cvt_pk_bf16(v0[0], v0[1]); w.y = cvt_pk_bf16(v0[2], v0[3]); w.z = cvt_pk_bf16(v1[0], v1[1]); w.w = cvt_pk_bf16(v1[2], v1[3]); return w; }
;     __device__ __forceinline__ void operator()(const f32x4 (&acc)[2][2][4][2], const Unit& u, int wr, int wc, int fr, int fq) const {
;     ...
; #pragma unroll
;         for (int ai = 0; ai < 2; ++ai)
; #pragma unroll
;             for (int m = 0; m < 4; ++m) {
;                 const int row = row0 + ai * HALF + m * 16; const float w = wv[ai][m];
; #pragma unroll
;                 for (int bj = 0; bj < 2; ++bj) *(u32x4*)(O + (size_t)(row - fr + tr_) * D + col0 - 8 * fq + 8 * tq_ + bj * HALF) = xpose4x16(pack8(acc[ai][bj][m][0] * w, acc[ai][bj][m][1] * w), sa_);
;             }
	global_store_dwordx4 v[166:167], v[88:91], off
	v_cvt_pk_bf16_f32 v80, v80, v81
	v_cvt_pk_bf16_f32 v81, v82, v83
	v_cvt_pk_bf16_f32 v82, v72, v73
	v_cvt_pk_bf16_f32 v75, v74, v75
	ds_bpermute_b32 v72, v155, v80
	ds_bpermute_b32 v73, v155, v81
	ds_bpermute_b32 v74, v155, v82
	ds_bpermute_b32 v75, v155, v75
	v_pk_mul_f32 v[82:83], v[86:87], v[238:239] op_sel_hi:[1,0]
	v_lshlrev_b64 v[80:81], 11, v[168:169]
	v_pk_mul_f32 v[60:61], v[60:61], v[240:241] op_sel_hi:[1,0]
	v_pk_mul_f32 v[58:59], v[58:59], v[240:241] op_sel_hi:[1,0]
	s_waitcnt lgkmcnt(0)
	global_store_dwordx4 v[166:167], v[72:75], off offset:256
	v_pk_mul_f32 v[56:57], v[56:57], v[240:241] op_sel_hi:[1,0]
	v_pk_mul_f32 v[54:55], v[54:55], v[240:241] op_sel_hi:[1,0]
	v_pk_mul_f32 v[74:75], v[76:77], v[238:239] op_sel_hi:[1,0]
	v_pk_mul_f32 v[72:73], v[78:79], v[238:239] op_sel_hi:[1,0]
	v_cvt_pk_bf16_f32 v76, v84, v85
	v_cvt_pk_bf16_f32 v77, v82, v83
	v_cvt_pk_bf16_f32 v74, v74, v75
	ds_bpermute_b32 v74, v155, v74
	v_cvt_pk_bf16_f32 v75, v72, v73
	ds_bpermute_b32 v72, v155, v76
	ds_bpermute_b32 v73, v155, v77
	ds_bpermute_b32 v75, v155, v75
	v_lshl_add_u64 v[76:77], s[4:5], 0, v[80:81]
	v_lshl_add_u64 v[76:77], v[76:77], 0, v[146:147]
	v_lshl_add_u64 v[76:77], v[76:77], 0, v[142:143]
	v_lshl_add_u64 v[76:77], v[76:77], 0, v[136:137]
	s_waitcnt lgkmcnt(0)
	global_store_dwordx4 v[76:77], v[72:75], off
	v_cvt_pk_bf16_f32 v68, v68, v69
	v_cvt_pk_bf16_f32 v69, v70, v71
	v_cvt_pk_bf16_f32 v70, v64, v65
	v_cvt_pk_bf16_f32 v67, v66, v67
	ds_bpermute_b32 v64, v155, v68
	ds_bpermute_b32 v65, v155, v69
	ds_bpermute_b32 v66, v155, v70
	ds_bpermute_b32 v67, v155, v67
	v_pk_mul_f32 v[52:53], v[52:53], v[240:241] op_sel_hi:[1,0]
	v_pk_mul_f32 v[50:51], v[50:51], v[240:241] op_sel_hi:[1,0]
	v_pk_mul_f32 v[48:49], v[48:49], v[240:241] op_sel_hi:[1,0]
	v_pk_mul_f32 v[46:47], v[46:47], v[242:243] op_sel_hi:[1,0]
	s_waitcnt lgkmcnt(0)
	global_store_dwordx4 v[76:77], v[64:67], off offset:256
	v_cvt_pk_bf16_f32 v60, v60, v61
	v_cvt_pk_bf16_f32 v61, v62, v63
	v_cvt_pk_bf16_f32 v62, v56, v57
	v_cvt_pk_bf16_f32 v59, v58, v59
	ds_bpermute_b32 v56, v155, v60
	s_nop 0
	v_add_u32_e32 v64, 0x80, v144
	v_ashrrev_i32_e32 v65, 31, v64
	v_lshlrev_b64 v[64:65], 11, v[64:65]
	ds_bpermute_b32 v57, v155, v61
	ds_bpermute_b32 v58, v155, v62
	ds_bpermute_b32 v59, v155, v59
	v_lshl_add_u64 v[60:61], s[4:5], 0, v[64:65]
	v_lshl_add_u64 v[60:61], v[60:61], 0, v[146:147]
	v_lshl_add_u64 v[60:61], v[60:61], 0, v[142:143]
	v_lshl_add_u64 v[60:61], v[60:61], 0, v[136:137]
	s_waitcnt lgkmcnt(0)
	global_store_dwordx4 v[60:61], v[56:59], off
	v_cvt_pk_bf16_f32 v52, v52, v53
	v_cvt_pk_bf16_f32 v53, v54, v55
	v_cvt_pk_bf16_f32 v54, v48, v49
	v_cvt_pk_bf16_f32 v51, v50, v51
	ds_bpermute_b32 v48, v155, v52
	ds_bpermute_b32 v49, v155, v53
	ds_bpermute_b32 v50, v155, v54
	ds_bpermute_b32 v51, v155, v51
	v_pk_mul_f32 v[44:45], v[44:45], v[242:243] op_sel_hi:[1,0]
	v_pk_mul_f32 v[42:43], v[42:43], v[242:243] op_sel_hi:[1,0]
	v_pk_mul_f32 v[40:41], v[40:41], v[242:243] op_sel_hi:[1,0]
	v_pk_mul_f32 v[38:39], v[38:39], v[242:243] op_sel_hi:[1,0]
	s_waitcnt lgkmcnt(0)
	global_store_dwordx4 v[60:61], v[48:51], off offset:256
	v_cvt_pk_bf16_f32 v44, v44, v45
	v_cvt_pk_bf16_f32 v45, v46, v47
	v_cvt_pk_bf16_f32 v46, v40, v41
	v_cvt_pk_bf16_f32 v43, v42, v43
	ds_bpermute_b32 v40, v155, v44
	s_nop 0
	v_add_u32_e32 v48, 0x90, v144
	v_ashrrev_i32_e32 v49, 31, v48
	v_lshlrev_b64 v[48:49], 11, v[48:49]
	ds_bpermute_b32 v41, v155, v45
	ds_bpermute_b32 v42, v155, v46
	ds_bpermute_b32 v43, v155, v43
	v_lshl_add_u64 v[44:45], s[4:5], 0, v[48:49]
	v_lshl_add_u64 v[44:45], v[44:45], 0, v[146:147]
	v_lshl_add_u64 v[44:45], v[44:45], 0, v[142:143]
	v_lshl_add_u64 v[44:45], v[44:45], 0, v[136:137]
	v_pk_mul_f32 v[36:37], v[36:37], v[242:243] op_sel_hi:[1,0]
	v_pk_mul_f32 v[34:35], v[34:35], v[242:243] op_sel_hi:[1,0]
	s_waitcnt lgkmcnt(0)
; #define PG8_BAR __builtin_amdgcn_s_barrier()
; __device__ __forceinline__ u32x4 pack8(const f32x4 v0, const f32x4 v1) { u32x4 w; w.x = cvt_pk_bf16(v0[0], v0[1]); w.y = cvt_pk_bf16(v0[2], v0[3]); w.z = cvt_pk_bf16(v1[0], v1[1]); w.w = cvt_pk_bf16(v1[2], v1[3]); return w; }
; template <class Epi, class Sched, class AM, bool ALIGN_EPI = false, bool SP2 = false>
; __device__ __forceinline__ void gemm_phase(PG8_LAS unsigned char* lds, const Gemm g, const Sched& S, const Epi& E, const AM& am, const int wid_in) {
;     ...
;         cur = nxt; cA = nA; cB = nB; ++ui;
;         if constexpr (AM::GATHER) { _Pragma("unroll") for (int h = 0; h < 2; ++h) _Pragma("unroll") for (int i = 0; i < 2; ++i) gao[h][i] = gno[h][i]; }
;         if constexpr (ALIGN_EPI) { if (wr == 1) PG8_BAR; }
;     __device__ __forceinline__ void operator()(const f32x4 (&acc)[2][2][4][2], const Unit& u, int wr, int wc, int fr, int fq) const {
;     ...
; #pragma unroll
;         for (int ai = 0; ai < 2; ++ai)
; #pragma unroll
;             for (int m = 0; m < 4; ++m) {
;                 const int row = row0 + ai * HALF + m * 16; const float w = wv[ai][m];
; #pragma unroll
;                 for (int bj = 0; bj < 2; ++bj) *(u32x4*)(O + (size_t)(row - fr + tr_) * D + col0 - 8 * fq + 8 * tq_ + bj * HALF) = xpose4x16(pack8(acc[ai][bj][m][0] * w, acc[ai][bj][m][1] * w), sa_);
;             }
	global_store_dwordx4 v[44:45], v[40:43], off
	v_pk_mul_f32 v[32:33], v[32:33], v[242:243] op_sel_hi:[1,0]
	v_cvt_pk_bf16_f32 v36, v36, v37
	v_cvt_pk_bf16_f32 v37, v38, v39
	v_pk_mul_f32 v[30:31], v[30:31], v[244:245] op_sel_hi:[1,0]
	v_cvt_pk_bf16_f32 v38, v32, v33
	v_cvt_pk_bf16_f32 v35, v34, v35
	ds_bpermute_b32 v32, v155, v36
	ds_bpermute_b32 v33, v155, v37
	ds_bpermute_b32 v34, v155, v38
	ds_bpermute_b32 v35, v155, v35
	v_pk_mul_f32 v[28:29], v[28:29], v[244:245] op_sel_hi:[1,0]
	v_pk_mul_f32 v[26:27], v[26:27], v[244:245] op_sel_hi:[1,0]
	v_pk_mul_f32 v[24:25], v[24:25], v[244:245] op_sel_hi:[1,0]
	v_pk_mul_f32 v[22:23], v[22:23], v[244:245] op_sel_hi:[1,0]
	s_waitcnt lgkmcnt(0)
	global_store_dwordx4 v[44:45], v[32:35], off offset:256
	v_cvt_pk_bf16_f32 v28, v28, v29
	v_cvt_pk_bf16_f32 v29, v30, v31
	v_cvt_pk_bf16_f32 v30, v24, v25
	v_cvt_pk_bf16_f32 v27, v26, v27
	ds_bpermute_b32 v24, v155, v28
	s_nop 0
	v_add_u32_e32 v32, 0xa0, v144
	v_ashrrev_i32_e32 v33, 31, v32
	v_lshlrev_b64 v[32:33], 11, v[32:33]
	ds_bpermute_b32 v25, v155, v29
	ds_bpermute_b32 v26, v155, v30
	ds_bpermute_b32 v27, v155, v27
	v_lshl_add_u64 v[28:29], s[4:5], 0, v[32:33]
	v_lshl_add_u64 v[28:29], v[28:29], 0, v[146:147]
	v_lshl_add_u64 v[28:29], v[28:29], 0, v[142:143]
	v_lshl_add_u64 v[28:29], v[28:29], 0, v[136:137]
	v_pk_mul_f32 v[20:21], v[20:21], v[244:245] op_sel_hi:[1,0]
	v_pk_mul_f32 v[18:19], v[18:19], v[244:245] op_sel_hi:[1,0]
	s_waitcnt lgkmcnt(0)
	global_store_dwordx4 v[28:29], v[24:27], off
	v_pk_mul_f32 v[16:17], v[16:17], v[244:245] op_sel_hi:[1,0]
	v_cvt_pk_bf16_f32 v20, v20, v21
	v_cvt_pk_bf16_f32 v21, v22, v23
	v_pk_mul_f32 v[14:15], v[14:15], v[246:247] op_sel_hi:[1,0]
	v_cvt_pk_bf16_f32 v22, v16, v17
	v_cvt_pk_bf16_f32 v19, v18, v19
	ds_bpermute_b32 v16, v155, v20
	ds_bpermute_b32 v17, v155, v21
	ds_bpermute_b32 v18, v155, v22
	ds_bpermute_b32 v19, v155, v19
	v_pk_mul_f32 v[12:13], v[12:13], v[246:247] op_sel_hi:[1,0]
	v_pk_mul_f32 v[10:11], v[10:11], v[246:247] op_sel_hi:[1,0]
	v_pk_mul_f32 v[8:9], v[8:9], v[246:247] op_sel_hi:[1,0]
	v_pk_mul_f32 v[6:7], v[6:7], v[246:247] op_sel_hi:[1,0]
	s_waitcnt lgkmcnt(0)
	global_store_dwordx4 v[28:29], v[16:19], off offset:256
	v_cvt_pk_bf16_f32 v12, v12, v13
	v_cvt_pk_bf16_f32 v13, v14, v15
	v_cvt_pk_bf16_f32 v14, v8, v9
	v_cvt_pk_bf16_f32 v11, v10, v11
	ds_bpermute_b32 v8, v155, v12
	s_nop 0
	v_add_u32_e32 v16, 0xb0, v144
	v_ashrrev_i32_e32 v17, 31, v16
	v_lshlrev_b64 v[16:17], 11, v[16:17]
	ds_bpermute_b32 v9, v155, v13
	ds_bpermute_b32 v10, v155, v14
	ds_bpermute_b32 v11, v155, v11
	v_lshl_add_u64 v[12:13], s[4:5], 0, v[16:17]
	v_lshl_add_u64 v[12:13], v[12:13], 0, v[146:147]
	v_lshl_add_u64 v[12:13], v[12:13], 0, v[142:143]
	v_lshl_add_u64 v[12:13], v[12:13], 0, v[136:137]
	v_pk_mul_f32 v[4:5], v[4:5], v[246:247] op_sel_hi:[1,0]
	v_pk_mul_f32 v[2:3], v[2:3], v[246:247] op_sel_hi:[1,0]
	s_waitcnt lgkmcnt(0)
	global_store_dwordx4 v[12:13], v[8:11], off
	v_pk_mul_f32 v[0:1], v[0:1], v[246:247] op_sel_hi:[1,0]
	v_cvt_pk_bf16_f32 v4, v4, v5
	v_cvt_pk_bf16_f32 v5, v6, v7
	s_nop 0
	v_cvt_pk_bf16_f32 v6, v0, v1
	v_cvt_pk_bf16_f32 v3, v2, v3
	ds_bpermute_b32 v0, v155, v4
	ds_bpermute_b32 v1, v155, v5
	ds_bpermute_b32 v2, v155, v6
	ds_bpermute_b32 v3, v155, v3
	s_waitcnt lgkmcnt(0)
	global_store_dwordx4 v[12:13], v[0:3], off offset:256
	s_cbranch_vccnz .LBB0_2710
	s_andn2_b64 vcc, exec, s[2:3]
	s_cbranch_vccnz .LBB0_2709
	s_barrier
	s_branch .LBB0_2709
